# speedup vs baseline: 1.0199x; 1.0199x over previous
_Z11prep_kernelPKfS0_S0_S0_S0_S0_S0_S0_S0_PKiPDv8_DF16bS4_PfS5_S5_PiPt:
	s_cmpk_gt_i32 s2, 0x7f
	s_load_dwordx2 s[4:5], s[0:1], 0x40
	s_load_dwordx4 s[16:19], s[0:1], 0x0
	s_load_dwordx2 s[14:15], s[0:1], 0x10
	s_load_dwordx2 s[20:21], s[0:1], 0x20
	s_load_dwordx4 s[8:11], s[0:1], 0x30
	s_load_dwordx2 s[26:27], s[0:1], 0x48
	s_load_dwordx2 s[28:29], s[0:1], 0x80
	s_cselect_b64 s[6:7], -1, 0
	s_lshl_b32 s12, s2, 4
	s_add_i32 s3, s12, 0xfffff800
	s_cmpk_lt_i32 s2, 0x80
	s_cselect_b32 s22, s12, s3
	s_waitcnt lgkmcnt(0)
	s_cselect_b32 s13, s17, s19
	s_cselect_b32 s16, s16, s18
	s_cselect_b32 s21, s15, s21
	s_cselect_b32 s20, s14, s20
	s_ashr_i32 s23, s22, 31
	s_lshl_b64 s[14:15], s[22:23], 9
	s_add_u32 s14, s16, s14
	s_addc_u32 s15, s13, s15
	s_lshl_b32 s13, s2, 9
	s_and_b32 s13, s13, 0xe00
	s_add_i32 s19, s2, 1
	v_or_b32_e32 v131, s13, v0
	s_lshl_b32 s13, s19, 9
	s_and_b32 s13, s13, 0xe00
	s_add_i32 s18, s2, 2
	v_or_b32_e32 v132, s13, v0
	s_lshl_b32 s13, s18, 9
	s_and_b32 s13, s13, 0xe00
	s_add_i32 s17, s2, 3
	v_or_b32_e32 v133, s13, v0
	s_lshl_b32 s13, s17, 9
	s_and_b32 s13, s13, 0xe00
	s_add_i32 s16, s2, 4
	v_lshlrev_b32_e32 v2, 4, v0
	v_or_b32_e32 v134, s13, v0
	s_lshl_b32 s13, s16, 9
	global_load_dwordx4 v[14:17], v2, s[14:15] nt
	s_and_b32 s13, s13, 0xe00
	s_add_i32 s15, s2, 5
	v_or_b32_e32 v135, s13, v0
	s_lshl_b32 s13, s15, 9
	s_and_b32 s13, s13, 0xe00
	s_add_i32 s14, s2, 6
	v_or_b32_e32 v136, s13, v0
	s_lshl_b32 s13, s14, 9
	s_and_b32 s13, s13, 0xe00
	v_or_b32_e32 v137, s13, v0
	s_add_i32 s13, s2, 7
	v_and_b32_e32 v1, 15, v0
	s_lshl_b32 s22, s13, 9
	v_lshrrev_b32_e32 v128, 6, v0
	s_and_b32 s22, s22, 0xe00
	v_lshl_or_b32 v107, v128, 4, v1
	v_lshlrev_b32_e32 v6, 4, v131
	v_lshlrev_b32_e32 v7, 4, v132
	v_lshlrev_b32_e32 v18, 4, v133
	v_lshlrev_b32_e32 v19, 4, v134
	v_lshlrev_b32_e32 v26, 4, v135
	v_lshlrev_b32_e32 v27, 4, v136
	v_lshlrev_b32_e32 v38, 4, v137
	v_or_b32_e32 v138, s22, v0
	v_lshlrev_b32_e32 v106, 2, v107
	global_load_dwordx4 v[10:13], v6, s[20:21]
	global_load_dwordx4 v[2:5], v7, s[20:21]
	global_load_dwordx4 v[22:25], v18, s[20:21]
	s_nop 0
	global_load_dwordx4 v[6:9], v19, s[20:21]
	global_load_dwordx4 v[30:33], v26, s[20:21]
	s_nop 0
	global_load_dwordx4 v[18:21], v27, s[20:21]
	v_lshlrev_b32_e32 v39, 4, v138
	global_load_dwordx4 v[34:37], v38, s[20:21]
	global_load_dwordx4 v[26:29], v39, s[20:21]
	global_load_dword v129, v106, s[4:5]
	global_load_dword v130, v106, s[10:11]
	v_and_b32_e32 v126, 63, v0
	v_lshlrev_b32_e32 v127, 2, v0
	v_mov_b32_e32 v39, 0
	s_and_b64 vcc, exec, s[6:7]
	v_cmp_gt_u32_e64 s[4:5], 32, v126
	v_lshlrev_b32_e32 v108, 4, v126
	s_cbranch_vccz .LBB0_2
	s_load_dwordx2 s[10:11], s[0:1], 0x28
	s_load_dwordx2 s[20:21], s[0:1], 0x18
	v_mov_b32_e32 v109, v39
	s_waitcnt lgkmcnt(0)
	v_mov_b32_e32 v38, s11
	v_mov_b32_e32 v40, s21
	v_mov_b32_e32 v42, s10
	v_mov_b32_e32 v43, s20
	v_cndmask_b32_e64 v41, v38, v40, s[4:5]
	v_cndmask_b32_e64 v40, v42, v43, s[4:5]
	v_and_b32_e32 v38, 0x7c, v127
	s_lshl_b32 s4, s2, 3
	v_lshlrev_b32_e32 v38, 2, v38
	s_and_b32 s5, s4, 0x78
	v_lshl_add_u64 v[40:41], v[40:41], 0, v[38:39]
	v_or_b32_e32 v38, s5, v128
	s_lshl_b32 s10, s19, 3
	global_load_dwordx4 v[102:105], v[40:41], off
	v_lshl_add_u64 v[40:41], s[8:9], 0, v[108:109]
	v_lshlrev_b32_e32 v38, 10, v38
	s_and_b32 s10, s10, 0x78
	v_lshl_add_u64 v[42:43], v[40:41], 0, v[38:39]
	v_or_b32_e32 v38, s10, v128
	s_lshl_b32 s10, s18, 3
	v_lshlrev_b32_e32 v38, 10, v38
	s_and_b32 s10, s10, 0x78
	v_lshl_add_u64 v[44:45], v[40:41], 0, v[38:39]
	v_or_b32_e32 v38, s10, v128
	s_lshl_b32 s10, s17, 3
	v_lshlrev_b32_e32 v38, 10, v38
	s_and_b32 s10, s10, 0x78
	global_load_dwordx4 v[98:101], v[42:43], off
	global_load_dwordx4 v[66:69], v[44:45], off
	v_lshl_add_u64 v[42:43], v[40:41], 0, v[38:39]
	v_or_b32_e32 v38, s10, v128
	s_lshl_b32 s10, s16, 3
	v_lshlrev_b32_e32 v38, 10, v38
	s_and_b32 s10, s10, 0x78
	v_lshl_add_u64 v[44:45], v[40:41], 0, v[38:39]
	v_or_b32_e32 v38, s10, v128
	s_lshl_b32 s10, s15, 3
	v_lshlrev_b32_e32 v38, 10, v38
	s_and_b32 s10, s10, 0x78
	global_load_dwordx4 v[94:97], v[42:43], off
	global_load_dwordx4 v[62:65], v[44:45], off
	v_lshl_add_u64 v[42:43], v[40:41], 0, v[38:39]
	v_or_b32_e32 v38, s10, v128
	s_lshl_b32 s10, s14, 3
	v_lshlrev_b32_e32 v38, 10, v38
	s_and_b32 s10, s10, 0x78
	v_lshl_add_u64 v[44:45], v[40:41], 0, v[38:39]
	v_or_b32_e32 v38, s10, v128
	s_lshl_b32 s10, s13, 3
	v_lshlrev_b32_e32 v38, 10, v38
	s_and_b32 s10, s10, 0x78
	global_load_dwordx4 v[90:93], v[42:43], off
	global_load_dwordx4 v[58:61], v[44:45], off
	v_lshl_add_u64 v[42:43], v[40:41], 0, v[38:39]
	v_or_b32_e32 v38, s10, v128
	v_lshlrev_b32_e32 v38, 10, v38
	v_lshl_add_u64 v[44:45], v[40:41], 0, v[38:39]
	v_bitop3_b32 v38, s5, v128, 64 bitop3:0xde
	s_add_i32 s5, s4, 0x48
	v_lshlrev_b32_e32 v38, 10, v38
	s_and_b32 s5, s5, 0x78
	global_load_dwordx4 v[86:89], v[42:43], off
	global_load_dwordx4 v[54:57], v[44:45], off
	v_lshl_add_u64 v[42:43], v[40:41], 0, v[38:39]
	v_or_b32_e32 v38, s5, v128
	s_add_i32 s5, s4, 0x50
	v_lshlrev_b32_e32 v38, 10, v38
	s_and_b32 s5, s5, 0x78
	v_lshl_add_u64 v[44:45], v[40:41], 0, v[38:39]
	v_or_b32_e32 v38, s5, v128
	s_add_i32 s5, s4, 0x58
	v_lshlrev_b32_e32 v38, 10, v38
	s_and_b32 s5, s5, 0x78
	global_load_dwordx4 v[82:85], v[42:43], off
	global_load_dwordx4 v[50:53], v[44:45], off
	v_lshl_add_u64 v[42:43], v[40:41], 0, v[38:39]
	v_or_b32_e32 v38, s5, v128
	s_add_i32 s5, s4, 0x60
	v_lshlrev_b32_e32 v38, 10, v38
	s_and_b32 s5, s5, 0x78
	v_lshl_add_u64 v[44:45], v[40:41], 0, v[38:39]
	v_or_b32_e32 v38, s5, v128
	s_add_i32 s5, s4, 0x68
	v_lshlrev_b32_e32 v38, 10, v38
	s_and_b32 s5, s5, 0x78
	v_lshl_add_u64 v[70:71], v[40:41], 0, v[38:39]
	v_or_b32_e32 v38, s5, v128
	s_add_i32 s5, s4, 0x70
	v_lshlrev_b32_e32 v38, 10, v38
	s_and_b32 s5, s5, 0x78
	v_lshl_add_u64 v[72:73], v[40:41], 0, v[38:39]
	v_or_b32_e32 v38, s5, v128
	s_addk_i32 s4, 0x78
	v_lshlrev_b32_e32 v38, 10, v38
	s_and_b32 s4, s4, 0x78
	v_lshl_add_u64 v[110:111], v[40:41], 0, v[38:39]
	v_or_b32_e32 v38, s4, v128
	v_lshlrev_b32_e32 v38, 10, v38
	global_load_dwordx4 v[78:81], v[42:43], off
	global_load_dwordx4 v[46:49], v[44:45], off
	global_load_dwordx4 v[74:77], v[70:71], off
	s_nop 0
	global_load_dwordx4 v[42:45], v[72:73], off
	v_lshl_add_u64 v[112:113], v[40:41], 0, v[38:39]
	global_load_dwordx4 v[70:73], v[110:111], off
	global_load_dwordx4 v[38:41], v[112:113], off
	s_mov_b64 s[4:5], 0
	s_andn2_b64 vcc, exec, s[4:5]
	s_cbranch_vccnz .LBB0_4
	s_branch .LBB0_3

.LBB0_8:
	s_andn2_b64 vcc, exec, s[8:9]
	s_waitcnt vmcnt(2)
	v_lshrrev_b32_e32 v45, 5, v131
	v_lshrrev_b32_e32 v44, 5, v132
	v_lshrrev_b32_e32 v43, 5, v133
	v_lshrrev_b32_e32 v42, 5, v134
	s_waitcnt vmcnt(0)
	v_lshrrev_b32_e32 v41, 5, v135
	v_lshrrev_b32_e32 v40, 5, v136
	v_lshrrev_b32_e32 v39, 5, v137
	v_lshrrev_b32_e32 v38, 5, v138
	s_cbranch_vccnz .LBB0_10
	v_and_b32_e32 v46, 0x7c, v127
	v_mov_b32_e32 v47, 0x8800
	v_lshl_or_b32 v46, v46, 1, v47
	s_movk_i32 s8, 0x110
	v_mad_u32_u24 v47, v45, s8, v46
	ds_write_b64 v47, v[110:111]
	v_mad_u32_u24 v47, v44, s8, v46
	ds_write_b64 v47, v[112:113]
	v_mad_u32_u24 v47, v43, s8, v46
	ds_write_b64 v47, v[114:115]
	v_mad_u32_u24 v47, v42, s8, v46
	ds_write_b64 v47, v[116:117]
	v_mad_u32_u24 v47, v41, s8, v46
	ds_write_b64 v47, v[118:119]
	v_mad_u32_u24 v47, v40, s8, v46
	ds_write_b64 v47, v[120:121]
	v_mad_u32_u24 v47, v39, s8, v46
	v_mad_u32_u24 v46, v38, s8, v46
	ds_write_b64 v47, v[122:123]
	ds_write_b64 v46, v[124:125]

.LBB0_40:
	s_cmp_lg_u32 s2, 0
	s_cbranch_scc1 .Lp_end
	v_mov_b32_e32 v44, s26
	v_mov_b32_e32 v45, s27
	v_mov_b32_e32 v46, 0
	s_mov_b64 exec, 1
	global_store_dwordx2 v46, v[44:45], s[28:29] sc1

_Z11main_kernelPKDv8_DF16bS1_PKfS3_S3_PKiPKtS3_S3_Pf:
	s_lshl_b32 s14, s2, 5
	s_load_dwordx4 s[4:7], s[0:1], 0x0
	s_load_dwordx2 s[36:37], s[0:1], 0x10
	s_load_dwordx4 s[8:11], s[0:1], 0x28
	s_and_b32 s3, s14, 0xe0
	s_lshr_b32 s33, s2, 3
	s_or_b32 s15, s3, s33
	v_lshrrev_b32_e32 v73, 6, v0
	s_lshl_b32 s34, s15, 3
	v_or_b32_e32 v54, s34, v73
	v_mov_b32_e32 v55, 0
	v_and_b32_e32 v1, 63, v0
	s_waitcnt lgkmcnt(0)
	s_load_dwordx2 s[50:51], s[10:11], 0x0
	v_and_b32_e32 v2, 7, v0
	v_bfe_u32 v74, v0, 4, 2
	v_lshlrev_b32_e32 v2, 4, v2
	s_mov_b32 s13, 0
	s_lshl_b32 s2, s15, 1
	s_lshl_b32 s12, s15, 2
	v_lshl_or_b32 v2, v74, 7, v2
	v_mov_b32_e32 v3, v55
	s_and_b32 s10, s2, 0x3ffffffc
	v_lshl_add_u64 v[58:59], s[4:5], 0, v[2:3]
	s_lshl_b64 s[2:3], s[12:13], 9
	v_lshl_add_u64 v[2:3], v[58:59], 0, s[2:3]
	s_or_b32 s2, s12, 1
	s_mov_b32 s3, s13
	s_lshl_b64 s[2:3], s[2:3], 9
	v_lshl_add_u64 v[4:5], v[58:59], 0, s[2:3]
	s_or_b32 s2, s12, 2
	s_mov_b32 s3, s13
	s_lshl_b64 s[2:3], s[2:3], 9
	global_load_dwordx4 v[22:25], v[2:3], off
	global_load_dwordx4 v[50:53], v[4:5], off
	v_lshl_add_u64 v[2:3], v[58:59], 0, s[2:3]
	s_or_b32 s2, s12, 3
	s_mov_b32 s3, s13
	s_lshl_b64 s[2:3], s[2:3], 9
	v_lshl_add_u64 v[4:5], v[58:59], 0, s[2:3]
	s_and_b32 s2, s14, 0x700
	s_add_i32 s5, s33, 1
	s_lshl_b32 s14, s2, 4
	s_lshl_b32 s2, s5, 8
	s_and_b32 s2, s2, 0x700
	s_add_i32 s38, s33, 2
	s_lshl_b32 s16, s2, 4
	s_lshl_b32 s2, s38, 8
	s_and_b32 s2, s2, 0x700
	s_add_i32 s39, s33, 3
	s_lshl_b32 s18, s2, 4
	s_lshl_b32 s2, s39, 8
	s_and_b32 s44, s15, 0x1fffff80
	v_lshlrev_b32_e32 v75, 3, v73
	s_and_b32 s2, s2, 0x700
	s_add_i32 s40, s33, 4
	global_load_dwordx4 v[60:63], v[2:3], off
	global_load_dwordx4 v[64:67], v[4:5], off
	v_or_b32_e32 v2, s44, v75
	v_mov_b32_e32 v3, v55
	s_lshl_b32 s20, s2, 4
	s_lshl_b32 s2, s40, 8
	v_lshlrev_b64 v[2:3], 12, v[2:3]
	s_and_b32 s2, s2, 0x700
	s_add_i32 s41, s33, 5
	v_lshl_add_u64 v[2:3], s[6:7], 0, v[2:3]
	v_lshlrev_b32_e32 v56, 4, v1
	v_mov_b32_e32 v57, v55
	s_lshl_b32 s22, s2, 4
	s_lshl_b32 s2, s41, 8
	v_lshl_add_u64 v[2:3], v[2:3], 0, v[56:57]
	s_mov_b32 s15, s13
	s_and_b32 s2, s2, 0x700
	s_add_i32 s42, s33, 6
	v_lshl_add_u64 v[4:5], v[2:3], 0, s[14:15]
	s_mov_b32 s17, s13
	s_lshl_b32 s24, s2, 4
	s_lshl_b32 s2, s42, 8
	global_load_dwordx4 v[18:21], v[4:5], off
	global_load_dwordx4 v[26:29], v[4:5], off offset:1024
	global_load_dwordx4 v[30:33], v[4:5], off offset:2048
	global_load_dwordx4 v[34:37], v[4:5], off offset:3072
	v_lshl_add_u64 v[4:5], v[2:3], 0, s[16:17]
	s_mov_b32 s19, s13
	s_and_b32 s2, s2, 0x700
	s_add_i32 s43, s33, 7
	global_load_dwordx4 v[38:41], v[4:5], off
	global_load_dwordx4 v[42:45], v[4:5], off offset:1024
	global_load_dwordx4 v[68:71], v[4:5], off offset:2048
	global_load_dwordx4 v[76:79], v[4:5], off offset:3072
	v_lshl_add_u64 v[4:5], v[2:3], 0, s[18:19]
	s_mov_b32 s21, s13
	s_lshl_b32 s26, s2, 4
	s_lshl_b32 s2, s43, 8
	global_load_dwordx4 v[80:83], v[4:5], off
	global_load_dwordx4 v[84:87], v[4:5], off offset:1024
	global_load_dwordx4 v[88:91], v[4:5], off offset:2048
	global_load_dwordx4 v[92:95], v[4:5], off offset:3072
	v_lshl_add_u64 v[4:5], v[2:3], 0, s[20:21]
	s_mov_b32 s23, s13
	s_and_b32 s2, s2, 0x700
	s_and_b32 s30, s34, 0x7ffffc00
	s_mov_b32 s31, s13
	global_load_dwordx4 v[96:99], v[4:5], off
	global_load_dwordx4 v[100:103], v[4:5], off offset:1024
	global_load_dwordx4 v[104:107], v[4:5], off offset:2048
	global_load_dwordx4 v[108:111], v[4:5], off offset:3072
	v_lshl_add_u64 v[4:5], v[2:3], 0, s[22:23]
	s_mov_b32 s25, s13
	s_lshl_b32 s28, s2, 4
	s_lshl_b64 s[2:3], s[30:31], 2
	global_load_dwordx4 v[112:115], v[4:5], off
	global_load_dwordx4 v[116:119], v[4:5], off offset:1024
	global_load_dwordx4 v[120:123], v[4:5], off offset:2048
	global_load_dwordx4 v[124:127], v[4:5], off offset:3072
	v_lshl_add_u64 v[4:5], v[2:3], 0, s[24:25]
	s_mov_b32 s27, s13
	s_mov_b32 s29, s13
	s_add_u32 s2, s36, s2
	global_load_dwordx4 v[128:131], v[4:5], off
	global_load_dwordx4 v[132:135], v[4:5], off offset:1024
	global_load_dwordx4 v[136:139], v[4:5], off offset:2048
	global_load_dwordx4 v[140:143], v[4:5], off offset:3072
	v_lshl_add_u64 v[4:5], v[2:3], 0, s[26:27]
	v_lshl_add_u64 v[2:3], v[2:3], 0, s[28:29]
	s_addc_u32 s3, s37, s3
	global_load_dwordx4 v[144:147], v[4:5], off
	global_load_dwordx4 v[148:151], v[4:5], off offset:1024
	global_load_dwordx4 v[152:155], v[4:5], off offset:2048
	global_load_dwordx4 v[156:159], v[4:5], off offset:3072
	global_load_dwordx4 v[160:163], v[2:3], off
	global_load_dwordx4 v[164:167], v[2:3], off offset:1024
	global_load_dwordx4 v[168:171], v[2:3], off offset:2048
	global_load_dwordx4 v[172:175], v[2:3], off offset:3072
	global_load_dwordx4 v[14:17], v56, s[2:3]
	global_load_dwordx4 v[10:13], v56, s[2:3] offset:1024
	global_load_dwordx4 v[6:9], v56, s[2:3] offset:2048
	s_nop 0
	global_load_dwordx4 v[2:5], v56, s[2:3] offset:3072
	s_load_dwordx2 s[2:3], s[0:1], 0x40
	s_load_dword s15, s[8:9], s10 offset:0x0
	v_lshlrev_b32_e32 v1, 2, v1
	s_waitcnt lgkmcnt(0)
	s_load_dword s4, s[2:3], 0x0
	v_lshl_add_u32 v220, v54, 12, v56
	global_load_dwordx4 v[204:207], v220, s[50:51] nt
	global_load_dwordx4 v[208:211], v220, s[50:51] offset:1024 nt
	global_load_dwordx4 v[212:215], v220, s[50:51] offset:2048 nt
	global_load_dwordx4 v[216:219], v220, s[50:51] offset:3072 nt
	s_cmp_lg_u32 s15, 1
	s_cbranch_scc1 .Lmy_generic
	s_load_dwordx2 s[0:1], s[0:1], 0x48
	s_mov_b64 s[2:3], -1
	v_lshlrev_b32_e32 v176, 9, v73
	s_movk_i32 s6, 0x4040
	v_and_b32_e32 v177, 15, v0
	v_mad_u32_u24 v176, v74, s6, v176
	v_lshl_or_b32 v176, v177, 2, v176
	s_lshl_b32 s6, s33, 6
	s_and_b32 s6, s6, 0x1c0
	v_add_u32_e32 v177, s6, v176
	s_lshl_b32 s6, s5, 6
	s_and_b32 s6, s6, 0x1c0
	v_add_u32_e32 v178, s6, v176
	s_lshl_b32 s6, s38, 6
	s_and_b32 s6, s6, 0x1c0
	v_add_u32_e32 v179, s6, v176
	s_lshl_b32 s6, s39, 6
	s_and_b32 s6, s6, 0x1c0
	v_add_u32_e32 v180, s6, v176
	s_lshl_b32 s6, s40, 6
	s_and_b32 s6, s6, 0x1c0
	v_add_u32_e32 v181, s6, v176
	s_lshl_b32 s6, s41, 6
	s_and_b32 s6, s6, 0x1c0
	v_add_u32_e32 v182, s6, v176
	s_lshl_b32 s6, s42, 6
	s_and_b32 s6, s6, 0x1c0
	v_add_u32_e32 v183, s6, v176
	s_lshl_b32 s6, s43, 6
	s_and_b32 s6, s6, 0x1c0
	v_add_u32_e32 v184, s6, v176
	s_waitcnt vmcnt(39)
	v_mfma_f32_16x16x32_bf16 v[18:21], v[22:25], v[18:21], 0
	s_waitcnt vmcnt(38)
	v_mfma_f32_16x16x32_bf16 v[18:21], v[50:53], v[26:29], v[18:21]
	s_waitcnt vmcnt(37)
	v_mfma_f32_16x16x32_bf16 v[18:21], v[60:63], v[30:33], v[18:21]
	s_waitcnt vmcnt(36)
	v_mfma_f32_16x16x32_bf16 v[46:49], v[64:67], v[34:37], v[18:21]
	s_waitcnt vmcnt(35)
	v_mfma_f32_16x16x32_bf16 v[18:21], v[22:25], v[38:41], 0
	s_waitcnt vmcnt(34)
	v_mfma_f32_16x16x32_bf16 v[18:21], v[50:53], v[42:45], v[18:21]
	s_waitcnt vmcnt(33)
	v_mfma_f32_16x16x32_bf16 v[18:21], v[60:63], v[68:71], v[18:21]
	s_waitcnt vmcnt(32)
	v_mfma_f32_16x16x32_bf16 v[42:45], v[64:67], v[76:79], v[18:21]
	ds_write_b32 v177, v46
	ds_write_b32 v177, v47 offset:4112
	ds_write_b32 v177, v48 offset:8224
	ds_write_b32 v177, v49 offset:12336
	s_waitcnt vmcnt(31)
	v_mfma_f32_16x16x32_bf16 v[18:21], v[22:25], v[80:83], 0
	s_waitcnt vmcnt(30)
	v_mfma_f32_16x16x32_bf16 v[18:21], v[50:53], v[84:87], v[18:21]
	s_waitcnt vmcnt(29)
	v_mfma_f32_16x16x32_bf16 v[18:21], v[60:63], v[88:91], v[18:21]
	s_waitcnt vmcnt(28)
	v_mfma_f32_16x16x32_bf16 v[38:41], v[64:67], v[92:95], v[18:21]
	ds_write_b32 v178, v42
	ds_write_b32 v178, v43 offset:4112
	ds_write_b32 v178, v44 offset:8224
	ds_write_b32 v178, v45 offset:12336
	s_waitcnt vmcnt(27)
	v_mfma_f32_16x16x32_bf16 v[18:21], v[22:25], v[96:99], 0
	s_waitcnt vmcnt(26)
	v_mfma_f32_16x16x32_bf16 v[18:21], v[50:53], v[100:103], v[18:21]
	s_waitcnt vmcnt(25)
	v_mfma_f32_16x16x32_bf16 v[18:21], v[60:63], v[104:107], v[18:21]
	s_waitcnt vmcnt(24)
	v_mfma_f32_16x16x32_bf16 v[34:37], v[64:67], v[108:111], v[18:21]
	ds_write_b32 v179, v38
	ds_write_b32 v179, v39 offset:4112
	ds_write_b32 v179, v40 offset:8224
	ds_write_b32 v179, v41 offset:12336
	s_waitcnt vmcnt(23)
	v_mfma_f32_16x16x32_bf16 v[18:21], v[22:25], v[112:115], 0
	s_waitcnt vmcnt(22)
	v_mfma_f32_16x16x32_bf16 v[18:21], v[50:53], v[116:119], v[18:21]
	s_waitcnt vmcnt(21)
	v_mfma_f32_16x16x32_bf16 v[18:21], v[60:63], v[120:123], v[18:21]
	s_waitcnt vmcnt(20)
	v_mfma_f32_16x16x32_bf16 v[30:33], v[64:67], v[124:127], v[18:21]
	ds_write_b32 v180, v34
	ds_write_b32 v180, v35 offset:4112
	ds_write_b32 v180, v36 offset:8224
	ds_write_b32 v180, v37 offset:12336
	s_waitcnt vmcnt(19)
	v_mfma_f32_16x16x32_bf16 v[18:21], v[22:25], v[128:131], 0
	s_waitcnt vmcnt(18)
	v_mfma_f32_16x16x32_bf16 v[18:21], v[50:53], v[132:135], v[18:21]
	s_waitcnt vmcnt(17)
	v_mfma_f32_16x16x32_bf16 v[18:21], v[60:63], v[136:139], v[18:21]
	s_waitcnt vmcnt(16)
	v_mfma_f32_16x16x32_bf16 v[26:29], v[64:67], v[140:143], v[18:21]
	ds_write_b32 v181, v30
	ds_write_b32 v181, v31 offset:4112
	ds_write_b32 v181, v32 offset:8224
	ds_write_b32 v181, v33 offset:12336
	s_waitcnt vmcnt(15)
	v_mfma_f32_16x16x32_bf16 v[18:21], v[22:25], v[144:147], 0
	s_waitcnt vmcnt(11)
	v_mfma_f32_16x16x32_bf16 v[22:25], v[22:25], v[160:163], 0
	v_mfma_f32_16x16x32_bf16 v[18:21], v[50:53], v[148:151], v[18:21]
	s_waitcnt vmcnt(10)
	v_mfma_f32_16x16x32_bf16 v[22:25], v[50:53], v[164:167], v[22:25]
	v_mfma_f32_16x16x32_bf16 v[18:21], v[60:63], v[152:155], v[18:21]
	s_waitcnt vmcnt(9)
	v_mfma_f32_16x16x32_bf16 v[22:25], v[60:63], v[168:171], v[22:25]
	ds_write_b32 v182, v26
	ds_write_b32 v182, v27 offset:4112
	ds_write_b32 v182, v28 offset:8224
	ds_write_b32 v182, v29 offset:12336
	v_mfma_f32_16x16x32_bf16 v[18:21], v[64:67], v[156:159], v[18:21]
	s_waitcnt vmcnt(8)
	v_mfma_f32_16x16x32_bf16 v[22:25], v[64:67], v[172:175], v[22:25]
	s_nop 7
	ds_write_b32 v183, v18
	ds_write_b32 v183, v19 offset:4112
	ds_write_b32 v183, v20 offset:8224
	ds_write_b32 v183, v21 offset:12336
	ds_write_b32 v184, v22
	ds_write_b32 v184, v23 offset:4112
	ds_write_b32 v184, v24 offset:8224
	ds_write_b32 v184, v25 offset:12336
	s_branch .LBB1_4

.LBB1_4:
	s_movk_i32 s5, 0x1010
	v_mad_u32_u24 v0, v73, s5, v56
	s_waitcnt lgkmcnt(0)
	s_barrier
	ds_read_b128 v[18:21], v0
	s_waitcnt vmcnt(3)
	v_pk_add_f32 v[22:23], s[4:5], v[16:17] op_sel_hi:[0,1]
	v_pk_add_f32 v[24:25], s[4:5], v[14:15] op_sel_hi:[0,1]
	ds_read_b128 v[14:17], v0 offset:1024
	s_waitcnt vmcnt(2)
	v_pk_add_f32 v[12:13], s[4:5], v[12:13] op_sel_hi:[0,1]
	s_waitcnt lgkmcnt(1)
	v_pk_add_f32 v[22:23], v[20:21], v[22:23]
	v_pk_add_f32 v[24:25], v[18:19], v[24:25]
	v_pk_add_f32 v[10:11], s[4:5], v[10:11] op_sel_hi:[0,1]
	v_cndmask_b32_e64 v21, v21, v23, s[2:3]
	v_cndmask_b32_e64 v20, v20, v22, s[2:3]
	v_cndmask_b32_e64 v22, v19, v25, s[2:3]
	v_cndmask_b32_e64 v23, v18, v24, s[2:3]
	s_waitcnt lgkmcnt(0)
	v_pk_add_f32 v[12:13], v[16:17], v[12:13]
	v_pk_add_f32 v[18:19], v[14:15], v[10:11]
	v_cndmask_b32_e64 v24, v17, v13, s[2:3]
	v_cndmask_b32_e64 v25, v16, v12, s[2:3]
	v_cndmask_b32_e64 v19, v15, v19, s[2:3]
	ds_read_b128 v[10:13], v0 offset:2048
	v_cndmask_b32_e64 v18, v14, v18, s[2:3]
	s_waitcnt vmcnt(1)
	v_pk_add_f32 v[14:15], s[4:5], v[8:9] op_sel_hi:[0,1]
	v_pk_add_f32 v[16:17], s[4:5], v[6:7] op_sel_hi:[0,1]
	ds_read_b128 v[6:9], v0 offset:3072
	s_waitcnt vmcnt(0)
	v_pk_add_f32 v[4:5], s[4:5], v[4:5] op_sel_hi:[0,1]
	v_mov_b32_e32 v72, 0
	v_cmp_ne_u32_e64 s[52:53], 0, v219
	v_cmp_ne_u32_e64 s[54:55], 0, v218
	v_cmp_ne_u32_e64 s[56:57], 0, v217
	v_cmp_ne_u32_e64 s[58:59], 0, v216
	v_addc_co_u32_e64 v72, s[60:61], v72, v72, s[52:53]
	v_addc_co_u32_e64 v72, s[60:61], v72, v72, s[54:55]
	v_addc_co_u32_e64 v72, s[60:61], v72, v72, s[56:57]
	v_addc_co_u32_e64 v72, s[60:61], v72, v72, s[58:59]
	v_cmp_ne_u32_e64 s[52:53], 0, v215
	v_cmp_ne_u32_e64 s[54:55], 0, v214
	v_cmp_ne_u32_e64 s[56:57], 0, v213
	v_cmp_ne_u32_e64 s[58:59], 0, v212
	v_addc_co_u32_e64 v72, s[60:61], v72, v72, s[52:53]
	v_addc_co_u32_e64 v72, s[60:61], v72, v72, s[54:55]
	v_addc_co_u32_e64 v72, s[60:61], v72, v72, s[56:57]
	v_addc_co_u32_e64 v72, s[60:61], v72, v72, s[58:59]
	v_cmp_ne_u32_e64 s[52:53], 0, v211
	v_cmp_ne_u32_e64 s[54:55], 0, v210
	v_cmp_ne_u32_e64 s[56:57], 0, v209
	v_cmp_ne_u32_e64 s[58:59], 0, v208
	v_addc_co_u32_e64 v72, s[60:61], v72, v72, s[52:53]
	v_addc_co_u32_e64 v72, s[60:61], v72, v72, s[54:55]
	v_addc_co_u32_e64 v72, s[60:61], v72, v72, s[56:57]
	v_addc_co_u32_e64 v72, s[60:61], v72, v72, s[58:59]
	v_cmp_ne_u32_e64 s[52:53], 0, v207
	v_cmp_ne_u32_e64 s[54:55], 0, v206
	v_cmp_ne_u32_e64 s[56:57], 0, v205
	v_cmp_ne_u32_e64 s[58:59], 0, v204
	v_addc_co_u32_e64 v72, s[60:61], v72, v72, s[52:53]
	v_addc_co_u32_e64 v72, s[60:61], v72, v72, s[54:55]
	v_addc_co_u32_e64 v72, s[60:61], v72, v72, s[56:57]
	v_addc_co_u32_e64 v72, s[60:61], v72, v72, s[58:59]
	v_cmp_ne_u16_e32 vcc, 0, v72
	s_cmp_lg_u64 vcc, 0
	v_and_b32_e32 v26, 0xffff, v72
	s_waitcnt lgkmcnt(0)
	v_pk_add_f32 v[4:5], v[8:9], v[4:5]
	s_cselect_b64 vcc, -1, 0
	v_cndmask_b32_e64 v4, v8, v4, s[2:3]
	v_mov_b32_e32 v8, 0xffff
	v_pk_add_f32 v[14:15], v[12:13], v[14:15]
	v_cndmask_b32_e32 v8, v8, v26, vcc
	v_cndmask_b32_e64 v0, v13, v15, s[2:3]
	v_and_b32_e32 v13, 1, v8
	v_pk_add_f32 v[16:17], v[10:11], v[16:17]
	v_cndmask_b32_e64 v12, v12, v14, s[2:3]
	v_cndmask_b32_e64 v5, v9, v5, s[2:3]
	v_mul_f32_e32 v9, 0x3fb8aa3b, v23
	v_mov_b32_e32 v14, 0xff800000
	v_cmp_eq_u32_e32 vcc, 1, v13
	v_and_b32_e32 v15, 2, v8
	v_cndmask_b32_e64 v11, v11, v17, s[2:3]
	v_cndmask_b32_e32 v9, v14, v9, vcc
	v_mul_f32_e32 v13, 0x3fb8aa3b, v22
	v_cmp_ne_u32_e32 vcc, 0, v15
	v_and_b32_e32 v17, 4, v8
	v_cndmask_b32_e64 v10, v10, v16, s[2:3]
	v_cndmask_b32_e32 v13, v14, v13, vcc
	v_mul_f32_e32 v16, 0x3fb8aa3b, v20
	v_cmp_ne_u32_e32 vcc, 0, v17
	v_and_b32_e32 v20, 8, v8
	v_mul_f32_e32 v17, 0x3fb8aa3b, v21
	v_cndmask_b32_e32 v16, v14, v16, vcc
	v_cmp_ne_u32_e32 vcc, 0, v20
	v_and_b32_e32 v20, 16, v8
	v_pk_add_f32 v[2:3], s[4:5], v[2:3] op_sel_hi:[0,1]
	v_cndmask_b32_e32 v17, v14, v17, vcc
	v_mul_f32_e32 v18, 0x3fb8aa3b, v18
	v_cmp_ne_u32_e32 vcc, 0, v20
	v_and_b32_e32 v20, 32, v8
	v_pk_add_f32 v[2:3], v[6:7], v[2:3]
	v_cndmask_b32_e32 v18, v14, v18, vcc
	v_mul_f32_e32 v19, 0x3fb8aa3b, v19
	v_cmp_ne_u32_e32 vcc, 0, v20
	v_and_b32_e32 v21, 64, v8
	v_cndmask_b32_e64 v7, v7, v3, s[2:3]
	v_cndmask_b32_e64 v6, v6, v2, s[2:3]
	v_lshlrev_b64 v[2:3], 12, v[54:55]
	v_cndmask_b32_e32 v19, v14, v19, vcc
	v_mul_f32_e32 v20, 0x3fb8aa3b, v25
	v_cmp_ne_u32_e32 vcc, 0, v21
	v_and_b32_e32 v22, 0x80, v8
	v_lshl_add_u64 v[2:3], s[0:1], 0, v[2:3]
	s_mov_b32 s0, 0xff800000
	v_cndmask_b32_e32 v20, v14, v20, vcc
	v_mul_f32_e32 v21, 0x3fb8aa3b, v24
	v_cmp_ne_u32_e32 vcc, 0, v22
	v_and_b32_e32 v22, 0x100, v8
	v_max3_f32 v15, v9, s0, v13
	v_cndmask_b32_e32 v21, v14, v21, vcc
	v_mul_f32_e32 v10, 0x3fb8aa3b, v10
	v_cmp_ne_u32_e32 vcc, 0, v22
	v_max3_f32 v15, v15, v16, v17
	v_max3_f32 v15, v15, v18, v19
	v_cndmask_b32_e32 v22, v14, v10, vcc
	v_mul_f32_e32 v10, 0x3fb8aa3b, v11
	v_and_b32_e32 v11, 0x200, v8
	v_cmp_ne_u32_e32 vcc, 0, v11
	v_mul_f32_e32 v11, 0x3fb8aa3b, v12
	v_and_b32_e32 v12, 0x400, v8
	v_max3_f32 v15, v15, v20, v21
	v_cndmask_b32_e32 v23, v14, v10, vcc
	v_cmp_ne_u32_e32 vcc, 0, v12
	v_max3_f32 v10, v15, v22, v23
	v_mul_f32_e32 v0, 0x3fb8aa3b, v0
	v_cndmask_b32_e32 v15, v14, v11, vcc
	v_and_b32_e32 v11, 0x800, v8
	v_cmp_ne_u32_e32 vcc, 0, v11
	v_and_b32_e32 v11, 0x1000, v8
	v_mul_f32_e32 v6, 0x3fb8aa3b, v6
	v_cndmask_b32_e32 v0, v14, v0, vcc
	v_cmp_ne_u32_e32 vcc, 0, v11
	v_mul_f32_e32 v4, 0x3fb8aa3b, v4
	s_movk_i32 s0, 0x7fff
	v_cndmask_b32_e32 v24, v14, v6, vcc
	v_mul_f32_e32 v6, 0x3fb8aa3b, v7
	v_and_b32_e32 v7, 0x2000, v8
	v_cmp_ne_u32_e32 vcc, 0, v7
	v_and_b32_e32 v7, 0x4000, v8
	v_max3_f32 v10, v10, v15, v0
	v_cndmask_b32_e32 v25, v14, v6, vcc
	v_cmp_ne_u32_e32 vcc, 0, v7
	v_max3_f32 v6, v10, v24, v25
	s_nop 0
	v_cndmask_b32_e32 v26, v14, v4, vcc
	v_mul_f32_e32 v4, 0x3fb8aa3b, v5
	v_cmp_lt_u32_e32 vcc, s0, v8
	v_mov_b32_e32 v5, 0
	s_nop 0
	v_cndmask_b32_e32 v27, v14, v4, vcc
	v_max3_f32 v4, v6, v26, v27
	s_nop 1
	v_mov_b32_dpp v5, v4 quad_perm:[1,0,3,2] row_mask:0xf bank_mask:0xf
	v_max_f32_e32 v5, v5, v5
	v_max_f32_e32 v4, v4, v5
	v_mov_b32_e32 v5, 0
	s_nop 1
	v_mov_b32_dpp v5, v4 quad_perm:[2,3,0,1] row_mask:0xf bank_mask:0xf
	v_max_f32_e32 v5, v5, v5
	v_max_f32_e32 v4, v4, v5
	v_mov_b32_e32 v5, 0
	s_nop 1
	v_mov_b32_dpp v5, v4 row_half_mirror row_mask:0xf bank_mask:0xf
	v_max_f32_e32 v5, v5, v5
	v_max_f32_e32 v4, v4, v5
	v_mov_b32_e32 v5, 0
	s_nop 1
	v_mov_b32_dpp v5, v4 row_mirror row_mask:0xf bank_mask:0xf
	v_max_f32_e32 v5, v5, v5
	v_max_f32_e32 v4, v4, v5
	s_nop 0
	v_readlane_b32 s2, v4, 32
	v_readlane_b32 s3, v4, 48
	v_readlane_b32 s0, v4, 0
	v_readlane_b32 s1, v4, 16
	v_max_f32_e64 v4, s3, s3
	v_max_f32_e64 v5, s2, s2
	v_max_f32_e32 v4, v5, v4
	v_mov_b32_e32 v5, s1
	v_max3_f32 v28, s0, v5, v4
	v_sub_f32_e32 v4, v9, v28
	v_exp_f32_e32 v4, v4
	v_sub_f32_e32 v5, v13, v28
	v_exp_f32_e32 v5, v5
	v_sub_f32_e32 v6, v16, v28
	v_exp_f32_e32 v6, v6
	v_sub_f32_e32 v7, v17, v28
	v_exp_f32_e32 v7, v7
	v_add_f32_e32 v8, 0, v4
	v_add_f32_e32 v8, v8, v5
	v_add_f32_e32 v8, v8, v6
	v_add_f32_e32 v12, v8, v7
	v_sub_f32_e32 v8, v18, v28
	v_exp_f32_e32 v8, v8
	v_sub_f32_e32 v9, v19, v28
	v_exp_f32_e32 v9, v9
	v_sub_f32_e32 v10, v20, v28
	v_exp_f32_e32 v10, v10
	v_sub_f32_e32 v11, v21, v28
	v_exp_f32_e32 v11, v11
	v_add_f32_e32 v12, v12, v8
	v_add_f32_e32 v12, v12, v9
	v_add_f32_e32 v12, v12, v10
	v_add_f32_e32 v16, v12, v11
	v_sub_f32_e32 v12, v22, v28
	v_exp_f32_e32 v12, v12
	v_sub_f32_e32 v13, v23, v28
	v_exp_f32_e32 v13, v13
	v_sub_f32_e32 v14, v15, v28
	v_exp_f32_e32 v14, v14
	v_sub_f32_e32 v0, v0, v28
	v_exp_f32_e32 v15, v0
	v_add_f32_e32 v0, v16, v12
	v_sub_f32_e32 v16, v24, v28
	v_exp_f32_e32 v16, v16
	v_sub_f32_e32 v17, v25, v28
	v_add_f32_e32 v0, v0, v13
	v_exp_f32_e32 v17, v17
	v_sub_f32_e32 v18, v26, v28
	v_add_f32_e32 v0, v0, v14
	v_exp_f32_e32 v18, v18
	v_sub_f32_e32 v19, v27, v28
	v_add_f32_e32 v0, v0, v15
	v_exp_f32_e32 v19, v19
	v_add_f32_e32 v0, v0, v16
	v_add_f32_e32 v0, v0, v17
	v_add_f32_e32 v0, v0, v18
	v_add_f32_e32 v0, v0, v19
	s_nop 1
	v_add_f32_dpp v0, v0, v0 quad_perm:[1,0,3,2] row_mask:0xf bank_mask:0xf bound_ctrl:1
	s_nop 1
	v_add_f32_dpp v0, v0, v0 quad_perm:[2,3,0,1] row_mask:0xf bank_mask:0xf bound_ctrl:1
	s_nop 1
	v_add_f32_dpp v0, v0, v0 row_half_mirror row_mask:0xf bank_mask:0xf bound_ctrl:1
	s_nop 1
	v_add_f32_dpp v0, v0, v0 row_mirror row_mask:0xf bank_mask:0xf bound_ctrl:1
	s_nop 0
	v_readlane_b32 s2, v0, 16
	v_readlane_b32 s3, v0, 48
	v_readlane_b32 s0, v0, 0
	v_readlane_b32 s1, v0, 32
	v_mov_b32_e32 v20, s2
	v_mov_b32_e32 v21, s3
	v_pk_add_f32 v[20:21], s[0:1], v[20:21]
	s_nop 0
	v_add_f32_e32 v0, v20, v21
	v_div_scale_f32 v22, s[0:1], v0, v0, 1.0
	v_rcp_f32_e32 v23, v22
	v_lshlrev_b32_e32 v20, 2, v1
	v_mov_b32_e32 v21, 0
	v_lshl_add_u64 v[20:21], v[2:3], 0, v[20:21]
	v_fma_f32 v1, -v22, v23, 1.0
	v_fmac_f32_e32 v23, v1, v23
	v_div_scale_f32 v1, vcc, 1.0, v0, 1.0
	v_mul_f32_e32 v2, v1, v23
	v_fma_f32 v3, -v22, v2, v1
	v_fmac_f32_e32 v2, v3, v23
	v_fma_f32 v1, -v22, v2, v1
	v_div_fmas_f32 v1, v1, v23, v2
	v_div_fixup_f32 v22, v1, v0, 1.0
	v_pk_mul_f32 v[2:3], v[22:23], v[6:7] op_sel_hi:[0,1]
	v_pk_mul_f32 v[0:1], v[22:23], v[4:5] op_sel_hi:[0,1]
	global_store_dwordx4 v[20:21], v[0:3], off sc1
	s_nop 1
	v_pk_mul_f32 v[2:3], v[22:23], v[10:11] op_sel_hi:[0,1]
	v_pk_mul_f32 v[0:1], v[22:23], v[8:9] op_sel_hi:[0,1]
	global_store_dwordx4 v[20:21], v[0:3], off offset:1024 sc1
	s_nop 1
	v_pk_mul_f32 v[2:3], v[22:23], v[14:15] op_sel_hi:[0,1]
	v_pk_mul_f32 v[0:1], v[22:23], v[12:13] op_sel_hi:[0,1]
	global_store_dwordx4 v[20:21], v[0:3], off offset:2048 sc1
	s_nop 1
	v_pk_mul_f32 v[2:3], v[22:23], v[18:19] op_sel_hi:[0,1]
	v_pk_mul_f32 v[0:1], v[22:23], v[16:17] op_sel_hi:[0,1]
	global_store_dwordx4 v[20:21], v[0:3], off offset:3072 sc1
	s_endpgm

	.amdhsa_kernel _Z11main_kernelPKDv8_DF16bS1_PKfS3_S3_PKiPKtS3_S3_Pf
		.amdhsa_group_segment_fixed_size 70400
		.amdhsa_private_segment_fixed_size 0
		.amdhsa_kernarg_size 80
		.amdhsa_user_sgpr_count 2
		.amdhsa_user_sgpr_dispatch_ptr 0
		.amdhsa_user_sgpr_queue_ptr 0
		.amdhsa_user_sgpr_kernarg_segment_ptr 1
		.amdhsa_user_sgpr_dispatch_id 0
		.amdhsa_user_sgpr_kernarg_preload_length 0
		.amdhsa_user_sgpr_kernarg_preload_offset 0
		.amdhsa_user_sgpr_private_segment_size 0
		.amdhsa_uses_dynamic_stack 0
		.amdhsa_enable_private_segment 0
		.amdhsa_system_sgpr_workgroup_id_x 1
		.amdhsa_system_sgpr_workgroup_id_y 0
		.amdhsa_system_sgpr_workgroup_id_z 0
		.amdhsa_system_sgpr_workgroup_info 0
		.amdhsa_system_vgpr_workitem_id 0
		.amdhsa_next_free_vgpr 224
		.amdhsa_next_free_sgpr 96
		.amdhsa_accum_offset 224
		.amdhsa_reserve_vcc 1
		.amdhsa_float_round_mode_32 0
		.amdhsa_float_round_mode_16_64 0
		.amdhsa_float_denorm_mode_32 3
		.amdhsa_float_denorm_mode_16_64 3
		.amdhsa_dx10_clamp 1
		.amdhsa_ieee_mode 1
		.amdhsa_fp16_overflow 0
		.amdhsa_tg_split 0
		.amdhsa_exception_fp_ieee_invalid_op 0
		.amdhsa_exception_fp_denorm_src 0
		.amdhsa_exception_fp_ieee_div_zero 0
		.amdhsa_exception_fp_ieee_overflow 0
		.amdhsa_exception_fp_ieee_underflow 0
		.amdhsa_exception_fp_ieee_inexact 0
		.amdhsa_exception_int_div_zero 0
	.end_amdhsa_kernel

amdhsa.kernels:
  - .agpr_count:     0
    .args:
      - .actual_access:  read_only
        .address_space:  global
        .offset:         0
        .size:           8
        .value_kind:     global_buffer
      - .actual_access:  read_only
        .address_space:  global
        .offset:         8
        .size:           8
        .value_kind:     global_buffer
      - .actual_access:  read_only
        .address_space:  global
        .offset:         16
        .size:           8
        .value_kind:     global_buffer
      - .actual_access:  read_only
        .address_space:  global
        .offset:         24
        .size:           8
        .value_kind:     global_buffer
      - .actual_access:  read_only
        .address_space:  global
        .offset:         32
        .size:           8
        .value_kind:     global_buffer
      - .actual_access:  read_only
        .address_space:  global
        .offset:         40
        .size:           8
        .value_kind:     global_buffer
      - .actual_access:  read_only
        .address_space:  global
        .offset:         48
        .size:           8
        .value_kind:     global_buffer
      - .actual_access:  read_only
        .address_space:  global
        .offset:         56
        .size:           8
        .value_kind:     global_buffer
      - .actual_access:  read_only
        .address_space:  global
        .offset:         64
        .size:           8
        .value_kind:     global_buffer
      - .actual_access:  read_only
        .address_space:  global
        .offset:         72
        .size:           8
        .value_kind:     global_buffer
      - .actual_access:  write_only
        .address_space:  global
        .offset:         80
        .size:           8
        .value_kind:     global_buffer
      - .actual_access:  write_only
        .address_space:  global
        .offset:         88
        .size:           8
        .value_kind:     global_buffer
      - .actual_access:  write_only
        .address_space:  global
        .offset:         96
        .size:           8
        .value_kind:     global_buffer
      - .actual_access:  write_only
        .address_space:  global
        .offset:         104
        .size:           8
        .value_kind:     global_buffer
      - .actual_access:  write_only
        .address_space:  global
        .offset:         112
        .size:           8
        .value_kind:     global_buffer
      - .actual_access:  write_only
        .address_space:  global
        .offset:         120
        .size:           8
        .value_kind:     global_buffer
      - .actual_access:  write_only
        .address_space:  global
        .offset:         128
        .size:           8
        .value_kind:     global_buffer
    .group_segment_fixed_size: 121344
    .kernarg_segment_align: 8
    .kernarg_segment_size: 136
    .language:       OpenCL C
    .language_version:
      - 2
      - 0
    .max_flat_workgroup_size: 512
    .name:           _Z11prep_kernelPKfS0_S0_S0_S0_S0_S0_S0_S0_PKiPDv8_DF16bS4_PfS5_S5_PiPt
    .private_segment_fixed_size: 0
    .sgpr_count:     31
    .sgpr_spill_count: 0
    .symbol:         _Z11prep_kernelPKfS0_S0_S0_S0_S0_S0_S0_S0_PKiPDv8_DF16bS4_PfS5_S5_PiPt.kd
    .uniform_work_group_size: 1
    .uses_dynamic_stack: false
    .vgpr_count:     142
    .vgpr_spill_count: 0
    .wavefront_size: 64
  - .agpr_count:     0
    .args:
      - .actual_access:  read_only
        .address_space:  global
        .offset:         0
        .size:           8
        .value_kind:     global_buffer
      - .actual_access:  read_only
        .address_space:  global
        .offset:         8
        .size:           8
        .value_kind:     global_buffer
      - .actual_access:  read_only
        .address_space:  global
        .offset:         16
        .size:           8
        .value_kind:     global_buffer
      - .actual_access:  read_only
        .address_space:  global
        .offset:         24
        .size:           8
        .value_kind:     global_buffer
      - .actual_access:  read_only
        .address_space:  global
        .offset:         32
        .size:           8
        .value_kind:     global_buffer
      - .actual_access:  read_only
        .address_space:  global
        .offset:         40
        .size:           8
        .value_kind:     global_buffer
      - .actual_access:  read_only
        .address_space:  global
        .offset:         48
        .size:           8
        .value_kind:     global_buffer
      - .actual_access:  read_only
        .address_space:  global
        .offset:         56
        .size:           8
        .value_kind:     global_buffer
      - .actual_access:  read_only
        .address_space:  global
        .offset:         64
        .size:           8
        .value_kind:     global_buffer
      - .actual_access:  write_only
        .address_space:  global
        .offset:         72
        .size:           8
        .value_kind:     global_buffer
    .group_segment_fixed_size: 70400
    .kernarg_segment_align: 8
    .kernarg_segment_size: 80
    .language:       OpenCL C
    .language_version:
      - 2
      - 0
    .max_flat_workgroup_size: 512
    .name:           _Z11main_kernelPKDv8_DF16bS1_PKfS3_S3_PKiPKtS3_S3_Pf
    .private_segment_fixed_size: 0
    .sgpr_count:     54
    .sgpr_spill_count: 0
    .symbol:         _Z11main_kernelPKDv8_DF16bS1_PKfS3_S3_PKiPKtS3_S3_Pf.kd
    .uniform_work_group_size: 1
    .uses_dynamic_stack: false
    .vgpr_count:     224
    .vgpr_spill_count: 0
    .wavefront_size: 64
